# prologue de-serialisation 2: conv-front per-item Z row staging issues its 8 conditional 16-B loads together, one wait, then 8 masked ds_write_b128 (was 8 dependent round trips)
# baseline (speedup 1.0000x reference)
; #define GAS __attribute__((address_space(1)))
; #define LAS __attribute__((address_space(3)))
; __device__ __forceinline__ void convpre_phase(const Ctx& C, const bf16* Z, const float* dw_w, const float* dw_b, const float* ln_g, const float* ln_b, bf16* ZC) {
;     ...
;     for (int item = C.blk; item < T / 32; item += C.G) {
;         const int t0 = item * 32, s0 = t0 & (SEQ - 1);
;         __syncthreads();
; #pragma unroll
;         for (int i = 0; i < 8; ++i) { const int task = C.tid + 512 * i, rr = task >> 6, ch = task & 63;
;             if (rr < 62) { v4u z = {0u, 0u, 0u, 0u};
;                 if (s0 - 30 + rr >= 0) z = *(const GAS v4u*)(Z + (size_t)(t0 - 30 + rr) * CONV_CH + 8 * ch);
;                 *(LAS v4u*)(zs + rr * 512 + 8 * ch) = z; } }
;         __syncthreads();
.LBB0_478:
	s_lshl_b32 s21, s20, 5
	s_and_b32 s0, s21, 0x7e0
	s_sub_i32 s23, 29, s0
	s_sub_i32 s22, s21, 30
	s_waitcnt lgkmcnt(0)
	s_barrier
	v_cmp_lt_i32_e32 vcc, s23, v98
	v_mov_b32_e32 v60, 0
	v_mov_b32_e32 v61, 0
	v_mov_b32_e32 v62, 0
	v_mov_b32_e32 v63, 0
	s_and_b64 vcc, vcc, s[2:3]
	s_and_saveexec_b64 s[18:19], vcc
	v_add_u32_e32 v60, s22, v98
	v_ashrrev_i32_e32 v61, 31, v60
	v_lshlrev_b64 v[60:61], 10, v[60:61]
	v_lshl_add_u64 v[60:61], v[0:1], 0, v[60:61]
	global_load_dwordx4 v[60:63], v[60:61], off
	s_or_b64 exec, exec, s[18:19]
	v_cmp_lt_i32_e32 vcc, s23, v99
	v_mov_b32_e32 v64, 0
	v_mov_b32_e32 v65, 0
	v_mov_b32_e32 v66, 0
	v_mov_b32_e32 v67, 0
	s_and_b64 vcc, vcc, s[4:5]
	s_and_saveexec_b64 s[18:19], vcc
	v_add_u32_e32 v64, s22, v99
	v_ashrrev_i32_e32 v65, 31, v64
	v_lshlrev_b64 v[64:65], 10, v[64:65]
	v_lshl_add_u64 v[64:65], v[0:1], 0, v[64:65]
	global_load_dwordx4 v[64:67], v[64:65], off
	s_or_b64 exec, exec, s[18:19]
	v_cmp_lt_i32_e32 vcc, s23, v100
	v_mov_b32_e32 v68, 0
	v_mov_b32_e32 v69, 0
	v_mov_b32_e32 v70, 0
	v_mov_b32_e32 v71, 0
	s_and_b64 vcc, vcc, s[6:7]
	s_and_saveexec_b64 s[18:19], vcc
	v_add_u32_e32 v68, s22, v100
	v_ashrrev_i32_e32 v69, 31, v68
	v_lshlrev_b64 v[68:69], 10, v[68:69]
	v_lshl_add_u64 v[68:69], v[0:1], 0, v[68:69]
	global_load_dwordx4 v[68:71], v[68:69], off
	s_or_b64 exec, exec, s[18:19]
	v_cmp_lt_i32_e32 vcc, s23, v101
	v_mov_b32_e32 v72, 0
	v_mov_b32_e32 v73, 0
	v_mov_b32_e32 v74, 0
	v_mov_b32_e32 v75, 0
	s_and_b64 vcc, vcc, s[8:9]
	s_and_saveexec_b64 s[18:19], vcc
	v_add_u32_e32 v72, s22, v101
	v_ashrrev_i32_e32 v73, 31, v72
	v_lshlrev_b64 v[72:73], 10, v[72:73]
	v_lshl_add_u64 v[72:73], v[0:1], 0, v[72:73]
	global_load_dwordx4 v[72:75], v[72:73], off
	s_or_b64 exec, exec, s[18:19]
	v_cmp_lt_i32_e32 vcc, s23, v102
	v_mov_b32_e32 v76, 0
	v_mov_b32_e32 v77, 0
	v_mov_b32_e32 v78, 0
	v_mov_b32_e32 v79, 0
	s_and_b64 vcc, vcc, s[10:11]
	s_and_saveexec_b64 s[18:19], vcc
	v_add_u32_e32 v76, s22, v102
	v_ashrrev_i32_e32 v77, 31, v76
	v_lshlrev_b64 v[76:77], 10, v[76:77]
	v_lshl_add_u64 v[76:77], v[0:1], 0, v[76:77]
	global_load_dwordx4 v[76:79], v[76:77], off
	s_or_b64 exec, exec, s[18:19]
	v_cmp_lt_i32_e32 vcc, s23, v103
	v_mov_b32_e32 v80, 0
	v_mov_b32_e32 v81, 0
	v_mov_b32_e32 v82, 0
	v_mov_b32_e32 v83, 0
	s_and_b64 vcc, vcc, s[12:13]
	s_and_saveexec_b64 s[18:19], vcc
	v_add_u32_e32 v80, s22, v103
	v_ashrrev_i32_e32 v81, 31, v80
	v_lshlrev_b64 v[80:81], 10, v[80:81]
	v_lshl_add_u64 v[80:81], v[0:1], 0, v[80:81]
	global_load_dwordx4 v[80:83], v[80:81], off
	s_or_b64 exec, exec, s[18:19]
	v_cmp_lt_i32_e32 vcc, s23, v104
	v_mov_b32_e32 v84, 0
	v_mov_b32_e32 v85, 0
	v_mov_b32_e32 v86, 0
	v_mov_b32_e32 v87, 0
	s_and_b64 vcc, vcc, s[14:15]
	s_and_saveexec_b64 s[18:19], vcc
	v_add_u32_e32 v84, s22, v104
	v_ashrrev_i32_e32 v85, 31, v84
	v_lshlrev_b64 v[84:85], 10, v[84:85]
	v_lshl_add_u64 v[84:85], v[0:1], 0, v[84:85]
	global_load_dwordx4 v[84:87], v[84:85], off
	s_or_b64 exec, exec, s[18:19]
	v_cmp_lt_i32_e32 vcc, s23, v105
	v_mov_b32_e32 v88, 0
	v_mov_b32_e32 v89, 0
	v_mov_b32_e32 v90, 0
	v_mov_b32_e32 v91, 0
	s_and_b64 vcc, vcc, s[16:17]
	s_and_saveexec_b64 s[18:19], vcc
	v_add_u32_e32 v88, s22, v105
	v_ashrrev_i32_e32 v89, 31, v88
	v_lshlrev_b64 v[88:89], 10, v[88:89]
	v_lshl_add_u64 v[88:89], v[0:1], 0, v[88:89]
	global_load_dwordx4 v[88:91], v[88:89], off
	s_or_b64 exec, exec, s[18:19]
	s_waitcnt vmcnt(0)
	s_and_saveexec_b64 s[0:1], s[2:3]
	ds_write_b128 v111, v[60:63] offset:63488
	s_or_b64 exec, exec, s[0:1]
	s_and_saveexec_b64 s[0:1], s[4:5]
	ds_write_b128 v112, v[64:67] offset:63488
	s_or_b64 exec, exec, s[0:1]
	s_and_saveexec_b64 s[0:1], s[6:7]
	ds_write_b128 v113, v[68:71] offset:63488
	s_or_b64 exec, exec, s[0:1]
	s_and_saveexec_b64 s[0:1], s[8:9]
	ds_write_b128 v114, v[72:75] offset:63488
	s_or_b64 exec, exec, s[0:1]
	s_and_saveexec_b64 s[0:1], s[10:11]
	ds_write_b128 v115, v[76:79] offset:63488
	s_or_b64 exec, exec, s[0:1]
	s_and_saveexec_b64 s[0:1], s[12:13]
	ds_write_b128 v116, v[80:83] offset:63488
	s_or_b64 exec, exec, s[0:1]
	s_and_saveexec_b64 s[0:1], s[14:15]
	ds_write_b128 v117, v[84:87] offset:63488
	s_or_b64 exec, exec, s[0:1]
	s_and_saveexec_b64 s[0:1], s[16:17]
	ds_write_b128 v118, v[88:91] offset:63488
